# S2 block-combine rewritten: fully unrolled 64-step chain with a 19-deep operand ring (loads issued 19 steps ahead), same arithmetic and stores
# speedup vs baseline: 1.0018x; 1.0011x over previous
.LBB0_637:
	s_lshl_b32 s1, s0, 9
	s_and_b32 s1, s1, 0xe00
	v_add_u32_e32 v104, s1, v64
	v_lshlrev_b32_e32 v104, 3, v104
	v_lshrrev_b32_e32 v105, 2, v64
	v_and_b32_e32 v105, 12, v105
	v_ashrrev_i32_e32 v106, 2, v64
	v_and_or_b32 v105, v106, -16, v105
	v_lshlrev_b32_e32 v105, 2, v105
	s_ashr_i32 s3, s0, 3
	s_mul_i32 s2, s3, 0x208000
	s_add_u32 s8, s4, s2
	s_addc_u32 s9, s5, 0
	s_add_u32 s10, s6, s2
	s_addc_u32 s11, s7, 0
	s_mul_i32 s2, s3, 0x8200
	s_add_u32 s12, s4, 0x8200000
	s_addc_u32 s13, s5, 0
	s_add_u32 s12, s12, s2
	s_addc_u32 s13, s13, 0
	s_movk_i32 s14, 0x8000
	s_mov_b32 s15, 0x8000
	s_movk_i32 s22, 0xfe00
	s_movk_i32 s23, 0x200
	s_bitcmp1_b32 s0, 3
	s_cselect_b32 s16, s14, s15
	s_cselect_b32 s17, -1, 0
	s_cselect_b32 s18, s22, s23
	s_cselect_b32 s19, -1, 0
	s_cselect_b32 s20, 64, 1
	s_lshl_b64 s[24:25], s[16:17], 1
	s_lshl_b32 s21, s20, 15
	s_lshl_b32 s20, s20, 9
	s_add_u32 s10, s10, s21
	s_addc_u32 s11, s11, 0
	v_mov_b32_e32 v112, 0
	v_mov_b32_e32 v113, 0
	v_mov_b32_e32 v114, 0
	v_mov_b32_e32 v115, 0
	global_load_dwordx4 v[0:3], v105, s[12:13]
	global_load_dwordx2 v[4:5], v104, s[8:9] nt
	s_add_u32 s8, s8, s21
	s_addc_u32 s9, s9, 0
	s_add_u32 s12, s12, s20
	s_addc_u32 s13, s13, 0
	global_load_dwordx4 v[6:9], v105, s[12:13]
	global_load_dwordx2 v[10:11], v104, s[8:9] nt
	s_add_u32 s8, s8, s16
	s_addc_u32 s9, s9, s17
	s_add_u32 s12, s12, s18
	s_addc_u32 s13, s13, s19
	global_load_dwordx4 v[12:15], v105, s[12:13]
	global_load_dwordx2 v[16:17], v104, s[8:9] nt
	s_add_u32 s8, s8, s16
	s_addc_u32 s9, s9, s17
	s_add_u32 s12, s12, s18
	s_addc_u32 s13, s13, s19
	global_load_dwordx4 v[18:21], v105, s[12:13]
	global_load_dwordx2 v[22:23], v104, s[8:9] nt
	s_add_u32 s8, s8, s16
	s_addc_u32 s9, s9, s17
	s_add_u32 s12, s12, s18
	s_addc_u32 s13, s13, s19
	global_load_dwordx4 v[24:27], v105, s[12:13]
	global_load_dwordx2 v[28:29], v104, s[8:9] nt
	s_add_u32 s8, s8, s16
	s_addc_u32 s9, s9, s17
	s_add_u32 s12, s12, s18
	s_addc_u32 s13, s13, s19
	global_load_dwordx4 v[30:33], v105, s[12:13]
	global_load_dwordx2 v[34:35], v104, s[8:9] nt
	s_add_u32 s8, s8, s16
	s_addc_u32 s9, s9, s17
	s_add_u32 s12, s12, s18
	s_addc_u32 s13, s13, s19
	global_load_dwordx4 v[36:39], v105, s[12:13]
	global_load_dwordx2 v[40:41], v104, s[8:9] nt
	s_add_u32 s8, s8, s16
	s_addc_u32 s9, s9, s17
	s_add_u32 s12, s12, s18
	s_addc_u32 s13, s13, s19
	global_load_dwordx4 v[42:45], v105, s[12:13]
	global_load_dwordx2 v[46:47], v104, s[8:9] nt
	s_add_u32 s8, s8, s16
	s_addc_u32 s9, s9, s17
	s_add_u32 s12, s12, s18
	s_addc_u32 s13, s13, s19
	global_load_dwordx4 v[48:51], v105, s[12:13]
	global_load_dwordx2 v[52:53], v104, s[8:9] nt
	s_add_u32 s8, s8, s16
	s_addc_u32 s9, s9, s17
	s_add_u32 s12, s12, s18
	s_addc_u32 s13, s13, s19
	global_load_dwordx4 v[54:57], v105, s[12:13]
	global_load_dwordx2 v[58:59], v104, s[8:9] nt
	s_add_u32 s8, s8, s16
	s_addc_u32 s9, s9, s17
	s_add_u32 s12, s12, s18
	s_addc_u32 s13, s13, s19
	global_load_dwordx4 v[60:63], v105, s[12:13]
	global_load_dwordx2 v[66:67], v104, s[8:9] nt
	s_add_u32 s8, s8, s16
	s_addc_u32 s9, s9, s17
	s_add_u32 s12, s12, s18
	s_addc_u32 s13, s13, s19
	global_load_dwordx4 v[72:75], v105, s[12:13]
	global_load_dwordx2 v[76:77], v104, s[8:9] nt
	s_add_u32 s8, s8, s16
	s_addc_u32 s9, s9, s17
	s_add_u32 s12, s12, s18
	s_addc_u32 s13, s13, s19
	global_load_dwordx4 v[78:81], v105, s[12:13]
	global_load_dwordx2 v[82:83], v104, s[8:9] nt
	s_add_u32 s8, s8, s16
	s_addc_u32 s9, s9, s17
	s_add_u32 s12, s12, s18
	s_addc_u32 s13, s13, s19
	global_load_dwordx4 v[84:87], v105, s[12:13]
	global_load_dwordx2 v[88:89], v104, s[8:9] nt
	s_add_u32 s8, s8, s16
	s_addc_u32 s9, s9, s17
	s_add_u32 s12, s12, s18
	s_addc_u32 s13, s13, s19
	global_load_dwordx4 v[90:93], v105, s[12:13]
	global_load_dwordx2 v[94:95], v104, s[8:9] nt
	s_add_u32 s8, s8, s16
	s_addc_u32 s9, s9, s17
	s_add_u32 s12, s12, s18
	s_addc_u32 s13, s13, s19
	global_load_dwordx4 v[96:99], v105, s[12:13]
	global_load_dwordx2 v[100:101], v104, s[8:9] nt
	s_add_u32 s8, s8, s16
	s_addc_u32 s9, s9, s17
	s_add_u32 s12, s12, s18
	s_addc_u32 s13, s13, s19
	global_load_dwordx4 v[244:247], v105, s[12:13]
	global_load_dwordx2 v[248:249], v104, s[8:9] nt
	s_add_u32 s8, s8, s16
	s_addc_u32 s9, s9, s17
	s_add_u32 s12, s12, s18
	s_addc_u32 s13, s13, s19
	global_load_dwordx4 v[250:253], v105, s[12:13]
	global_load_dwordx2 v[254:255], v104, s[8:9] nt
	s_add_u32 s8, s8, s16
	s_addc_u32 s9, s9, s17
	s_add_u32 s12, s12, s18
	s_addc_u32 s13, s13, s19
	global_load_dwordx4 v[196:199], v105, s[12:13]
	global_load_dwordx2 v[68:69], v104, s[8:9] nt
	s_add_u32 s8, s8, s16
	s_addc_u32 s9, s9, s17
	s_add_u32 s12, s12, s18
	s_addc_u32 s13, s13, s19
	s_waitcnt vmcnt(36)
	v_lshlrev_b32_e32 v108, 16, v4
	v_and_b32_e32 v109, 0xffff0000, v4
	v_lshlrev_b32_e32 v110, 16, v5
	v_and_b32_e32 v111, 0xffff0000, v5
	v_pk_fma_f32 v[112:113], v[0:1], v[112:113], v[108:109]
	v_pk_fma_f32 v[114:115], v[2:3], v[114:115], v[110:111]
	global_load_dwordx4 v[0:3], v105, s[12:13]
	global_load_dwordx2 v[4:5], v104, s[8:9] nt
	s_add_u32 s8, s8, s16
	s_addc_u32 s9, s9, s17
	s_add_u32 s12, s12, s18
	s_addc_u32 s13, s13, s19
	s_waitcnt vmcnt(36)
	v_cvt_pk_bf16_f32 v106, v112, v113
	v_cvt_pk_bf16_f32 v107, v114, v115
	global_store_dwordx2 v104, v[106:107], s[10:11]
	s_add_u32 s10, s10, s24
	s_addc_u32 s11, s11, s25
	v_lshlrev_b32_e32 v108, 16, v10
	v_and_b32_e32 v109, 0xffff0000, v10
	v_lshlrev_b32_e32 v110, 16, v11
	v_and_b32_e32 v111, 0xffff0000, v11
	v_pk_fma_f32 v[112:113], v[6:7], v[112:113], v[108:109]
	v_pk_fma_f32 v[114:115], v[8:9], v[114:115], v[110:111]
	global_load_dwordx4 v[6:9], v105, s[12:13]
	global_load_dwordx2 v[10:11], v104, s[8:9] nt
	s_add_u32 s8, s8, s16
	s_addc_u32 s9, s9, s17
	s_add_u32 s12, s12, s18
	s_addc_u32 s13, s13, s19
	s_waitcnt vmcnt(37)
	v_lshlrev_b32_e32 v108, 16, v16
	v_and_b32_e32 v109, 0xffff0000, v16
	v_lshlrev_b32_e32 v110, 16, v17
	v_and_b32_e32 v111, 0xffff0000, v17
	v_pk_fma_f32 v[112:113], v[12:13], v[112:113], v[108:109]
	v_pk_fma_f32 v[114:115], v[14:15], v[114:115], v[110:111]
	global_load_dwordx4 v[12:15], v105, s[12:13]
	global_load_dwordx2 v[16:17], v104, s[8:9] nt
	s_add_u32 s8, s8, s16
	s_addc_u32 s9, s9, s17
	s_add_u32 s12, s12, s18
	s_addc_u32 s13, s13, s19
	s_waitcnt vmcnt(37)
	v_cvt_pk_bf16_f32 v106, v112, v113
	v_cvt_pk_bf16_f32 v107, v114, v115
	global_store_dwordx2 v104, v[106:107], s[10:11]
	s_add_u32 s10, s10, s24
	s_addc_u32 s11, s11, s25
	v_lshlrev_b32_e32 v108, 16, v22
	v_and_b32_e32 v109, 0xffff0000, v22
	v_lshlrev_b32_e32 v110, 16, v23
	v_and_b32_e32 v111, 0xffff0000, v23
	v_pk_fma_f32 v[112:113], v[18:19], v[112:113], v[108:109]
	v_pk_fma_f32 v[114:115], v[20:21], v[114:115], v[110:111]
	global_load_dwordx4 v[18:21], v105, s[12:13]
	global_load_dwordx2 v[22:23], v104, s[8:9] nt
	s_add_u32 s8, s8, s16
	s_addc_u32 s9, s9, s17
	s_add_u32 s12, s12, s18
	s_addc_u32 s13, s13, s19
	s_waitcnt vmcnt(38)
	v_lshlrev_b32_e32 v108, 16, v28
	v_and_b32_e32 v109, 0xffff0000, v28
	v_lshlrev_b32_e32 v110, 16, v29
	v_and_b32_e32 v111, 0xffff0000, v29
	v_pk_fma_f32 v[112:113], v[24:25], v[112:113], v[108:109]
	v_pk_fma_f32 v[114:115], v[26:27], v[114:115], v[110:111]
	global_load_dwordx4 v[24:27], v105, s[12:13]
	global_load_dwordx2 v[28:29], v104, s[8:9] nt
	s_add_u32 s8, s8, s16
	s_addc_u32 s9, s9, s17
	s_add_u32 s12, s12, s18
	s_addc_u32 s13, s13, s19
	s_waitcnt vmcnt(38)
	v_cvt_pk_bf16_f32 v106, v112, v113
	v_cvt_pk_bf16_f32 v107, v114, v115
	global_store_dwordx2 v104, v[106:107], s[10:11]
	s_add_u32 s10, s10, s24
	s_addc_u32 s11, s11, s25
	v_lshlrev_b32_e32 v108, 16, v34
	v_and_b32_e32 v109, 0xffff0000, v34
	v_lshlrev_b32_e32 v110, 16, v35
	v_and_b32_e32 v111, 0xffff0000, v35
	v_pk_fma_f32 v[112:113], v[30:31], v[112:113], v[108:109]
	v_pk_fma_f32 v[114:115], v[32:33], v[114:115], v[110:111]
	global_load_dwordx4 v[30:33], v105, s[12:13]
	global_load_dwordx2 v[34:35], v104, s[8:9] nt
	s_add_u32 s8, s8, s16
	s_addc_u32 s9, s9, s17
	s_add_u32 s12, s12, s18
	s_addc_u32 s13, s13, s19
	s_waitcnt vmcnt(39)
	v_lshlrev_b32_e32 v108, 16, v40
	v_and_b32_e32 v109, 0xffff0000, v40
	v_lshlrev_b32_e32 v110, 16, v41
	v_and_b32_e32 v111, 0xffff0000, v41
	v_pk_fma_f32 v[112:113], v[36:37], v[112:113], v[108:109]
	v_pk_fma_f32 v[114:115], v[38:39], v[114:115], v[110:111]
	global_load_dwordx4 v[36:39], v105, s[12:13]
	global_load_dwordx2 v[40:41], v104, s[8:9] nt
	s_add_u32 s8, s8, s16
	s_addc_u32 s9, s9, s17
	s_add_u32 s12, s12, s18
	s_addc_u32 s13, s13, s19
	s_waitcnt vmcnt(39)
	v_cvt_pk_bf16_f32 v106, v112, v113
	v_cvt_pk_bf16_f32 v107, v114, v115
	global_store_dwordx2 v104, v[106:107], s[10:11]
	s_add_u32 s10, s10, s24
	s_addc_u32 s11, s11, s25
	v_lshlrev_b32_e32 v108, 16, v46
	v_and_b32_e32 v109, 0xffff0000, v46
	v_lshlrev_b32_e32 v110, 16, v47
	v_and_b32_e32 v111, 0xffff0000, v47
	v_pk_fma_f32 v[112:113], v[42:43], v[112:113], v[108:109]
	v_pk_fma_f32 v[114:115], v[44:45], v[114:115], v[110:111]
	global_load_dwordx4 v[42:45], v105, s[12:13]
	global_load_dwordx2 v[46:47], v104, s[8:9] nt
	s_add_u32 s8, s8, s16
	s_addc_u32 s9, s9, s17
	s_add_u32 s12, s12, s18
	s_addc_u32 s13, s13, s19
	s_waitcnt vmcnt(40)
	v_lshlrev_b32_e32 v108, 16, v52
	v_and_b32_e32 v109, 0xffff0000, v52
	v_lshlrev_b32_e32 v110, 16, v53
	v_and_b32_e32 v111, 0xffff0000, v53
	v_pk_fma_f32 v[112:113], v[48:49], v[112:113], v[108:109]
	v_pk_fma_f32 v[114:115], v[50:51], v[114:115], v[110:111]
	global_load_dwordx4 v[48:51], v105, s[12:13]
	global_load_dwordx2 v[52:53], v104, s[8:9] nt
	s_add_u32 s8, s8, s16
	s_addc_u32 s9, s9, s17
	s_add_u32 s12, s12, s18
	s_addc_u32 s13, s13, s19
	s_waitcnt vmcnt(40)
	v_cvt_pk_bf16_f32 v106, v112, v113
	v_cvt_pk_bf16_f32 v107, v114, v115
	global_store_dwordx2 v104, v[106:107], s[10:11]
	s_add_u32 s10, s10, s24
	s_addc_u32 s11, s11, s25
	v_lshlrev_b32_e32 v108, 16, v58
	v_and_b32_e32 v109, 0xffff0000, v58
	v_lshlrev_b32_e32 v110, 16, v59
	v_and_b32_e32 v111, 0xffff0000, v59
	v_pk_fma_f32 v[112:113], v[54:55], v[112:113], v[108:109]
	v_pk_fma_f32 v[114:115], v[56:57], v[114:115], v[110:111]
	global_load_dwordx4 v[54:57], v105, s[12:13]
	global_load_dwordx2 v[58:59], v104, s[8:9] nt
	s_add_u32 s8, s8, s16
	s_addc_u32 s9, s9, s17
	s_add_u32 s12, s12, s18
	s_addc_u32 s13, s13, s19
	s_waitcnt vmcnt(41)
	v_lshlrev_b32_e32 v108, 16, v66
	v_and_b32_e32 v109, 0xffff0000, v66
	v_lshlrev_b32_e32 v110, 16, v67
	v_and_b32_e32 v111, 0xffff0000, v67
	v_pk_fma_f32 v[112:113], v[60:61], v[112:113], v[108:109]
	v_pk_fma_f32 v[114:115], v[62:63], v[114:115], v[110:111]
	global_load_dwordx4 v[60:63], v105, s[12:13]
	global_load_dwordx2 v[66:67], v104, s[8:9] nt
	s_add_u32 s8, s8, s16
	s_addc_u32 s9, s9, s17
	s_add_u32 s12, s12, s18
	s_addc_u32 s13, s13, s19
	s_waitcnt vmcnt(41)
	v_cvt_pk_bf16_f32 v106, v112, v113
	v_cvt_pk_bf16_f32 v107, v114, v115
	global_store_dwordx2 v104, v[106:107], s[10:11]
	s_add_u32 s10, s10, s24
	s_addc_u32 s11, s11, s25
	v_lshlrev_b32_e32 v108, 16, v76
	v_and_b32_e32 v109, 0xffff0000, v76
	v_lshlrev_b32_e32 v110, 16, v77
	v_and_b32_e32 v111, 0xffff0000, v77
	v_pk_fma_f32 v[112:113], v[72:73], v[112:113], v[108:109]
	v_pk_fma_f32 v[114:115], v[74:75], v[114:115], v[110:111]
	global_load_dwordx4 v[72:75], v105, s[12:13]
	global_load_dwordx2 v[76:77], v104, s[8:9] nt
	s_add_u32 s8, s8, s16
	s_addc_u32 s9, s9, s17
	s_add_u32 s12, s12, s18
	s_addc_u32 s13, s13, s19
	s_waitcnt vmcnt(42)
	v_lshlrev_b32_e32 v108, 16, v82
	v_and_b32_e32 v109, 0xffff0000, v82
	v_lshlrev_b32_e32 v110, 16, v83
	v_and_b32_e32 v111, 0xffff0000, v83
	v_pk_fma_f32 v[112:113], v[78:79], v[112:113], v[108:109]
	v_pk_fma_f32 v[114:115], v[80:81], v[114:115], v[110:111]
	global_load_dwordx4 v[78:81], v105, s[12:13]
	global_load_dwordx2 v[82:83], v104, s[8:9] nt
	s_add_u32 s8, s8, s16
	s_addc_u32 s9, s9, s17
	s_add_u32 s12, s12, s18
	s_addc_u32 s13, s13, s19
	s_waitcnt vmcnt(42)
	v_cvt_pk_bf16_f32 v106, v112, v113
	v_cvt_pk_bf16_f32 v107, v114, v115
	global_store_dwordx2 v104, v[106:107], s[10:11]
	s_add_u32 s10, s10, s24
	s_addc_u32 s11, s11, s25
	v_lshlrev_b32_e32 v108, 16, v88
	v_and_b32_e32 v109, 0xffff0000, v88
	v_lshlrev_b32_e32 v110, 16, v89
	v_and_b32_e32 v111, 0xffff0000, v89
	v_pk_fma_f32 v[112:113], v[84:85], v[112:113], v[108:109]
	v_pk_fma_f32 v[114:115], v[86:87], v[114:115], v[110:111]
	global_load_dwordx4 v[84:87], v105, s[12:13]
	global_load_dwordx2 v[88:89], v104, s[8:9] nt
	s_add_u32 s8, s8, s16
	s_addc_u32 s9, s9, s17
	s_add_u32 s12, s12, s18
	s_addc_u32 s13, s13, s19
	s_waitcnt vmcnt(43)
	v_lshlrev_b32_e32 v108, 16, v94
	v_and_b32_e32 v109, 0xffff0000, v94
	v_lshlrev_b32_e32 v110, 16, v95
	v_and_b32_e32 v111, 0xffff0000, v95
	v_pk_fma_f32 v[112:113], v[90:91], v[112:113], v[108:109]
	v_pk_fma_f32 v[114:115], v[92:93], v[114:115], v[110:111]
	global_load_dwordx4 v[90:93], v105, s[12:13]
	global_load_dwordx2 v[94:95], v104, s[8:9] nt
	s_add_u32 s8, s8, s16
	s_addc_u32 s9, s9, s17
	s_add_u32 s12, s12, s18
	s_addc_u32 s13, s13, s19
	s_waitcnt vmcnt(43)
	v_cvt_pk_bf16_f32 v106, v112, v113
	v_cvt_pk_bf16_f32 v107, v114, v115
	global_store_dwordx2 v104, v[106:107], s[10:11]
	s_add_u32 s10, s10, s24
	s_addc_u32 s11, s11, s25
	v_lshlrev_b32_e32 v108, 16, v100
	v_and_b32_e32 v109, 0xffff0000, v100
	v_lshlrev_b32_e32 v110, 16, v101
	v_and_b32_e32 v111, 0xffff0000, v101
	v_pk_fma_f32 v[112:113], v[96:97], v[112:113], v[108:109]
	v_pk_fma_f32 v[114:115], v[98:99], v[114:115], v[110:111]
	global_load_dwordx4 v[96:99], v105, s[12:13]
	global_load_dwordx2 v[100:101], v104, s[8:9] nt
	s_add_u32 s8, s8, s16
	s_addc_u32 s9, s9, s17
	s_add_u32 s12, s12, s18
	s_addc_u32 s13, s13, s19
	s_waitcnt vmcnt(44)
	v_lshlrev_b32_e32 v108, 16, v248
	v_and_b32_e32 v109, 0xffff0000, v248
	v_lshlrev_b32_e32 v110, 16, v249
	v_and_b32_e32 v111, 0xffff0000, v249
	v_pk_fma_f32 v[112:113], v[244:245], v[112:113], v[108:109]
	v_pk_fma_f32 v[114:115], v[246:247], v[114:115], v[110:111]
	global_load_dwordx4 v[244:247], v105, s[12:13]
	global_load_dwordx2 v[248:249], v104, s[8:9] nt
	s_add_u32 s8, s8, s16
	s_addc_u32 s9, s9, s17
	s_add_u32 s12, s12, s18
	s_addc_u32 s13, s13, s19
	s_waitcnt vmcnt(44)
	v_cvt_pk_bf16_f32 v106, v112, v113
	v_cvt_pk_bf16_f32 v107, v114, v115
	global_store_dwordx2 v104, v[106:107], s[10:11]
	s_add_u32 s10, s10, s24
	s_addc_u32 s11, s11, s25
	v_lshlrev_b32_e32 v108, 16, v254
	v_and_b32_e32 v109, 0xffff0000, v254
	v_lshlrev_b32_e32 v110, 16, v255
	v_and_b32_e32 v111, 0xffff0000, v255
	v_pk_fma_f32 v[112:113], v[250:251], v[112:113], v[108:109]
	v_pk_fma_f32 v[114:115], v[252:253], v[114:115], v[110:111]
	global_load_dwordx4 v[250:253], v105, s[12:13]
	global_load_dwordx2 v[254:255], v104, s[8:9] nt
	s_add_u32 s8, s8, s16
	s_addc_u32 s9, s9, s17
	s_add_u32 s12, s12, s18
	s_addc_u32 s13, s13, s19
	s_waitcnt vmcnt(45)
	v_lshlrev_b32_e32 v108, 16, v68
	v_and_b32_e32 v109, 0xffff0000, v68
	v_lshlrev_b32_e32 v110, 16, v69
	v_and_b32_e32 v111, 0xffff0000, v69
	v_pk_fma_f32 v[112:113], v[196:197], v[112:113], v[108:109]
	v_pk_fma_f32 v[114:115], v[198:199], v[114:115], v[110:111]
	global_load_dwordx4 v[196:199], v105, s[12:13]
	global_load_dwordx2 v[68:69], v104, s[8:9] nt
	s_add_u32 s8, s8, s16
	s_addc_u32 s9, s9, s17
	s_add_u32 s12, s12, s18
	s_addc_u32 s13, s13, s19
	s_waitcnt vmcnt(45)
	v_cvt_pk_bf16_f32 v106, v112, v113
	v_cvt_pk_bf16_f32 v107, v114, v115
	global_store_dwordx2 v104, v[106:107], s[10:11]
	s_add_u32 s10, s10, s24
	s_addc_u32 s11, s11, s25
	v_lshlrev_b32_e32 v108, 16, v4
	v_and_b32_e32 v109, 0xffff0000, v4
	v_lshlrev_b32_e32 v110, 16, v5
	v_and_b32_e32 v111, 0xffff0000, v5
	v_pk_fma_f32 v[112:113], v[0:1], v[112:113], v[108:109]
	v_pk_fma_f32 v[114:115], v[2:3], v[114:115], v[110:111]
	global_load_dwordx4 v[0:3], v105, s[12:13]
	global_load_dwordx2 v[4:5], v104, s[8:9] nt
	s_add_u32 s8, s8, s16
	s_addc_u32 s9, s9, s17
	s_add_u32 s12, s12, s18
	s_addc_u32 s13, s13, s19
	s_waitcnt vmcnt(45)
	v_lshlrev_b32_e32 v108, 16, v10
	v_and_b32_e32 v109, 0xffff0000, v10
	v_lshlrev_b32_e32 v110, 16, v11
	v_and_b32_e32 v111, 0xffff0000, v11
	v_pk_fma_f32 v[112:113], v[6:7], v[112:113], v[108:109]
	v_pk_fma_f32 v[114:115], v[8:9], v[114:115], v[110:111]
	global_load_dwordx4 v[6:9], v105, s[12:13]
	global_load_dwordx2 v[10:11], v104, s[8:9] nt
	s_add_u32 s8, s8, s16
	s_addc_u32 s9, s9, s17
	s_add_u32 s12, s12, s18
	s_addc_u32 s13, s13, s19
	s_waitcnt vmcnt(45)
	v_cvt_pk_bf16_f32 v106, v112, v113
	v_cvt_pk_bf16_f32 v107, v114, v115
	global_store_dwordx2 v104, v[106:107], s[10:11]
	s_add_u32 s10, s10, s24
	s_addc_u32 s11, s11, s25
	v_lshlrev_b32_e32 v108, 16, v16
	v_and_b32_e32 v109, 0xffff0000, v16
	v_lshlrev_b32_e32 v110, 16, v17
	v_and_b32_e32 v111, 0xffff0000, v17
	v_pk_fma_f32 v[112:113], v[12:13], v[112:113], v[108:109]
	v_pk_fma_f32 v[114:115], v[14:15], v[114:115], v[110:111]
	global_load_dwordx4 v[12:15], v105, s[12:13]
	global_load_dwordx2 v[16:17], v104, s[8:9] nt
	s_add_u32 s8, s8, s16
	s_addc_u32 s9, s9, s17
	s_add_u32 s12, s12, s18
	s_addc_u32 s13, s13, s19
	s_waitcnt vmcnt(45)
	v_lshlrev_b32_e32 v108, 16, v22
	v_and_b32_e32 v109, 0xffff0000, v22
	v_lshlrev_b32_e32 v110, 16, v23
	v_and_b32_e32 v111, 0xffff0000, v23
	v_pk_fma_f32 v[112:113], v[18:19], v[112:113], v[108:109]
	v_pk_fma_f32 v[114:115], v[20:21], v[114:115], v[110:111]
	global_load_dwordx4 v[18:21], v105, s[12:13]
	global_load_dwordx2 v[22:23], v104, s[8:9] nt
	s_add_u32 s8, s8, s16
	s_addc_u32 s9, s9, s17
	s_add_u32 s12, s12, s18
	s_addc_u32 s13, s13, s19
	s_waitcnt vmcnt(45)
	v_cvt_pk_bf16_f32 v106, v112, v113
	v_cvt_pk_bf16_f32 v107, v114, v115
	global_store_dwordx2 v104, v[106:107], s[10:11]
	s_add_u32 s10, s10, s24
	s_addc_u32 s11, s11, s25
	v_lshlrev_b32_e32 v108, 16, v28
	v_and_b32_e32 v109, 0xffff0000, v28
	v_lshlrev_b32_e32 v110, 16, v29
	v_and_b32_e32 v111, 0xffff0000, v29
	v_pk_fma_f32 v[112:113], v[24:25], v[112:113], v[108:109]
	v_pk_fma_f32 v[114:115], v[26:27], v[114:115], v[110:111]
	global_load_dwordx4 v[24:27], v105, s[12:13]
	global_load_dwordx2 v[28:29], v104, s[8:9] nt
	s_add_u32 s8, s8, s16
	s_addc_u32 s9, s9, s17
	s_add_u32 s12, s12, s18
	s_addc_u32 s13, s13, s19
	s_waitcnt vmcnt(45)
	v_lshlrev_b32_e32 v108, 16, v34
	v_and_b32_e32 v109, 0xffff0000, v34
	v_lshlrev_b32_e32 v110, 16, v35
	v_and_b32_e32 v111, 0xffff0000, v35
	v_pk_fma_f32 v[112:113], v[30:31], v[112:113], v[108:109]
	v_pk_fma_f32 v[114:115], v[32:33], v[114:115], v[110:111]
	global_load_dwordx4 v[30:33], v105, s[12:13]
	global_load_dwordx2 v[34:35], v104, s[8:9] nt
	s_add_u32 s8, s8, s16
	s_addc_u32 s9, s9, s17
	s_add_u32 s12, s12, s18
	s_addc_u32 s13, s13, s19
	s_waitcnt vmcnt(45)
	v_cvt_pk_bf16_f32 v106, v112, v113
	v_cvt_pk_bf16_f32 v107, v114, v115
	global_store_dwordx2 v104, v[106:107], s[10:11]
	s_add_u32 s10, s10, s24
	s_addc_u32 s11, s11, s25
	v_lshlrev_b32_e32 v108, 16, v40
	v_and_b32_e32 v109, 0xffff0000, v40
	v_lshlrev_b32_e32 v110, 16, v41
	v_and_b32_e32 v111, 0xffff0000, v41
	v_pk_fma_f32 v[112:113], v[36:37], v[112:113], v[108:109]
	v_pk_fma_f32 v[114:115], v[38:39], v[114:115], v[110:111]
	global_load_dwordx4 v[36:39], v105, s[12:13]
	global_load_dwordx2 v[40:41], v104, s[8:9] nt
	s_add_u32 s8, s8, s16
	s_addc_u32 s9, s9, s17
	s_add_u32 s12, s12, s18
	s_addc_u32 s13, s13, s19
	s_waitcnt vmcnt(45)
	v_lshlrev_b32_e32 v108, 16, v46
	v_and_b32_e32 v109, 0xffff0000, v46
	v_lshlrev_b32_e32 v110, 16, v47
	v_and_b32_e32 v111, 0xffff0000, v47
	v_pk_fma_f32 v[112:113], v[42:43], v[112:113], v[108:109]
	v_pk_fma_f32 v[114:115], v[44:45], v[114:115], v[110:111]
	global_load_dwordx4 v[42:45], v105, s[12:13]
	global_load_dwordx2 v[46:47], v104, s[8:9] nt
	s_add_u32 s8, s8, s16
	s_addc_u32 s9, s9, s17
	s_add_u32 s12, s12, s18
	s_addc_u32 s13, s13, s19
	s_waitcnt vmcnt(45)
	v_cvt_pk_bf16_f32 v106, v112, v113
	v_cvt_pk_bf16_f32 v107, v114, v115
	global_store_dwordx2 v104, v[106:107], s[10:11]
	s_add_u32 s10, s10, s24
	s_addc_u32 s11, s11, s25
	v_lshlrev_b32_e32 v108, 16, v52
	v_and_b32_e32 v109, 0xffff0000, v52
	v_lshlrev_b32_e32 v110, 16, v53
	v_and_b32_e32 v111, 0xffff0000, v53
	v_pk_fma_f32 v[112:113], v[48:49], v[112:113], v[108:109]
	v_pk_fma_f32 v[114:115], v[50:51], v[114:115], v[110:111]
	global_load_dwordx4 v[48:51], v105, s[12:13]
	global_load_dwordx2 v[52:53], v104, s[8:9] nt
	s_add_u32 s8, s8, s16
	s_addc_u32 s9, s9, s17
	s_add_u32 s12, s12, s18
	s_addc_u32 s13, s13, s19
	s_waitcnt vmcnt(45)
	v_lshlrev_b32_e32 v108, 16, v58
	v_and_b32_e32 v109, 0xffff0000, v58
	v_lshlrev_b32_e32 v110, 16, v59
	v_and_b32_e32 v111, 0xffff0000, v59
	v_pk_fma_f32 v[112:113], v[54:55], v[112:113], v[108:109]
	v_pk_fma_f32 v[114:115], v[56:57], v[114:115], v[110:111]
	global_load_dwordx4 v[54:57], v105, s[12:13]
	global_load_dwordx2 v[58:59], v104, s[8:9] nt
	s_add_u32 s8, s8, s16
	s_addc_u32 s9, s9, s17
	s_add_u32 s12, s12, s18
	s_addc_u32 s13, s13, s19
	s_waitcnt vmcnt(45)
	v_cvt_pk_bf16_f32 v106, v112, v113
	v_cvt_pk_bf16_f32 v107, v114, v115
	global_store_dwordx2 v104, v[106:107], s[10:11]
	s_add_u32 s10, s10, s24
	s_addc_u32 s11, s11, s25
	v_lshlrev_b32_e32 v108, 16, v66
	v_and_b32_e32 v109, 0xffff0000, v66
	v_lshlrev_b32_e32 v110, 16, v67
	v_and_b32_e32 v111, 0xffff0000, v67
	v_pk_fma_f32 v[112:113], v[60:61], v[112:113], v[108:109]
	v_pk_fma_f32 v[114:115], v[62:63], v[114:115], v[110:111]
	global_load_dwordx4 v[60:63], v105, s[12:13]
	global_load_dwordx2 v[66:67], v104, s[8:9] nt
	s_add_u32 s8, s8, s16
	s_addc_u32 s9, s9, s17
	s_add_u32 s12, s12, s18
	s_addc_u32 s13, s13, s19
	s_waitcnt vmcnt(45)
	v_lshlrev_b32_e32 v108, 16, v76
	v_and_b32_e32 v109, 0xffff0000, v76
	v_lshlrev_b32_e32 v110, 16, v77
	v_and_b32_e32 v111, 0xffff0000, v77
	v_pk_fma_f32 v[112:113], v[72:73], v[112:113], v[108:109]
	v_pk_fma_f32 v[114:115], v[74:75], v[114:115], v[110:111]
	global_load_dwordx4 v[72:75], v105, s[12:13]
	global_load_dwordx2 v[76:77], v104, s[8:9] nt
	s_add_u32 s8, s8, s16
	s_addc_u32 s9, s9, s17
	s_add_u32 s12, s12, s18
	s_addc_u32 s13, s13, s19
	s_waitcnt vmcnt(45)
	v_cvt_pk_bf16_f32 v106, v112, v113
	v_cvt_pk_bf16_f32 v107, v114, v115
	global_store_dwordx2 v104, v[106:107], s[10:11]
	s_add_u32 s10, s10, s24
	s_addc_u32 s11, s11, s25
	v_lshlrev_b32_e32 v108, 16, v82
	v_and_b32_e32 v109, 0xffff0000, v82
	v_lshlrev_b32_e32 v110, 16, v83
	v_and_b32_e32 v111, 0xffff0000, v83
	v_pk_fma_f32 v[112:113], v[78:79], v[112:113], v[108:109]
	v_pk_fma_f32 v[114:115], v[80:81], v[114:115], v[110:111]
	global_load_dwordx4 v[78:81], v105, s[12:13]
	global_load_dwordx2 v[82:83], v104, s[8:9] nt
	s_add_u32 s8, s8, s16
	s_addc_u32 s9, s9, s17
	s_add_u32 s12, s12, s18
	s_addc_u32 s13, s13, s19
	s_waitcnt vmcnt(45)
	v_lshlrev_b32_e32 v108, 16, v88
	v_and_b32_e32 v109, 0xffff0000, v88
	v_lshlrev_b32_e32 v110, 16, v89
	v_and_b32_e32 v111, 0xffff0000, v89
	v_pk_fma_f32 v[112:113], v[84:85], v[112:113], v[108:109]
	v_pk_fma_f32 v[114:115], v[86:87], v[114:115], v[110:111]
	global_load_dwordx4 v[84:87], v105, s[12:13]
	global_load_dwordx2 v[88:89], v104, s[8:9] nt
	s_add_u32 s8, s8, s16
	s_addc_u32 s9, s9, s17
	s_add_u32 s12, s12, s18
	s_addc_u32 s13, s13, s19
	s_waitcnt vmcnt(45)
	v_cvt_pk_bf16_f32 v106, v112, v113
	v_cvt_pk_bf16_f32 v107, v114, v115
	global_store_dwordx2 v104, v[106:107], s[10:11]
	s_add_u32 s10, s10, s24
	s_addc_u32 s11, s11, s25
	v_lshlrev_b32_e32 v108, 16, v94
	v_and_b32_e32 v109, 0xffff0000, v94
	v_lshlrev_b32_e32 v110, 16, v95
	v_and_b32_e32 v111, 0xffff0000, v95
	v_pk_fma_f32 v[112:113], v[90:91], v[112:113], v[108:109]
	v_pk_fma_f32 v[114:115], v[92:93], v[114:115], v[110:111]
	global_load_dwordx4 v[90:93], v105, s[12:13]
	global_load_dwordx2 v[94:95], v104, s[8:9] nt
	s_add_u32 s8, s8, s16
	s_addc_u32 s9, s9, s17
	s_add_u32 s12, s12, s18
	s_addc_u32 s13, s13, s19
	s_waitcnt vmcnt(45)
	v_lshlrev_b32_e32 v108, 16, v100
	v_and_b32_e32 v109, 0xffff0000, v100
	v_lshlrev_b32_e32 v110, 16, v101
	v_and_b32_e32 v111, 0xffff0000, v101
	v_pk_fma_f32 v[112:113], v[96:97], v[112:113], v[108:109]
	v_pk_fma_f32 v[114:115], v[98:99], v[114:115], v[110:111]
	global_load_dwordx4 v[96:99], v105, s[12:13]
	global_load_dwordx2 v[100:101], v104, s[8:9] nt
	s_add_u32 s8, s8, s16
	s_addc_u32 s9, s9, s17
	s_add_u32 s12, s12, s18
	s_addc_u32 s13, s13, s19
	s_waitcnt vmcnt(45)
	v_cvt_pk_bf16_f32 v106, v112, v113
	v_cvt_pk_bf16_f32 v107, v114, v115
	global_store_dwordx2 v104, v[106:107], s[10:11]
	s_add_u32 s10, s10, s24
	s_addc_u32 s11, s11, s25
	v_lshlrev_b32_e32 v108, 16, v248
	v_and_b32_e32 v109, 0xffff0000, v248
	v_lshlrev_b32_e32 v110, 16, v249
	v_and_b32_e32 v111, 0xffff0000, v249
	v_pk_fma_f32 v[112:113], v[244:245], v[112:113], v[108:109]
	v_pk_fma_f32 v[114:115], v[246:247], v[114:115], v[110:111]
	global_load_dwordx4 v[244:247], v105, s[12:13]
	global_load_dwordx2 v[248:249], v104, s[8:9] nt
	s_add_u32 s8, s8, s16
	s_addc_u32 s9, s9, s17
	s_add_u32 s12, s12, s18
	s_addc_u32 s13, s13, s19
	s_waitcnt vmcnt(45)
	v_lshlrev_b32_e32 v108, 16, v254
	v_and_b32_e32 v109, 0xffff0000, v254
	v_lshlrev_b32_e32 v110, 16, v255
	v_and_b32_e32 v111, 0xffff0000, v255
	v_pk_fma_f32 v[112:113], v[250:251], v[112:113], v[108:109]
	v_pk_fma_f32 v[114:115], v[252:253], v[114:115], v[110:111]
	global_load_dwordx4 v[250:253], v105, s[12:13]
	global_load_dwordx2 v[254:255], v104, s[8:9] nt
	s_add_u32 s8, s8, s16
	s_addc_u32 s9, s9, s17
	s_add_u32 s12, s12, s18
	s_addc_u32 s13, s13, s19
	s_waitcnt vmcnt(45)
	v_cvt_pk_bf16_f32 v106, v112, v113
	v_cvt_pk_bf16_f32 v107, v114, v115
	global_store_dwordx2 v104, v[106:107], s[10:11]
	s_add_u32 s10, s10, s24
	s_addc_u32 s11, s11, s25
	v_lshlrev_b32_e32 v108, 16, v68
	v_and_b32_e32 v109, 0xffff0000, v68
	v_lshlrev_b32_e32 v110, 16, v69
	v_and_b32_e32 v111, 0xffff0000, v69
	v_pk_fma_f32 v[112:113], v[196:197], v[112:113], v[108:109]
	v_pk_fma_f32 v[114:115], v[198:199], v[114:115], v[110:111]
	global_load_dwordx4 v[196:199], v105, s[12:13]
	global_load_dwordx2 v[68:69], v104, s[8:9] nt
	s_add_u32 s8, s8, s16
	s_addc_u32 s9, s9, s17
	s_add_u32 s12, s12, s18
	s_addc_u32 s13, s13, s19
	s_waitcnt vmcnt(45)
	v_lshlrev_b32_e32 v108, 16, v4
	v_and_b32_e32 v109, 0xffff0000, v4
	v_lshlrev_b32_e32 v110, 16, v5
	v_and_b32_e32 v111, 0xffff0000, v5
	v_pk_fma_f32 v[112:113], v[0:1], v[112:113], v[108:109]
	v_pk_fma_f32 v[114:115], v[2:3], v[114:115], v[110:111]
	global_load_dwordx4 v[0:3], v105, s[12:13]
	global_load_dwordx2 v[4:5], v104, s[8:9] nt
	s_add_u32 s8, s8, s16
	s_addc_u32 s9, s9, s17
	s_add_u32 s12, s12, s18
	s_addc_u32 s13, s13, s19
	s_waitcnt vmcnt(45)
	v_cvt_pk_bf16_f32 v106, v112, v113
	v_cvt_pk_bf16_f32 v107, v114, v115
	global_store_dwordx2 v104, v[106:107], s[10:11]
	s_add_u32 s10, s10, s24
	s_addc_u32 s11, s11, s25
	v_lshlrev_b32_e32 v108, 16, v10
	v_and_b32_e32 v109, 0xffff0000, v10
	v_lshlrev_b32_e32 v110, 16, v11
	v_and_b32_e32 v111, 0xffff0000, v11
	v_pk_fma_f32 v[112:113], v[6:7], v[112:113], v[108:109]
	v_pk_fma_f32 v[114:115], v[8:9], v[114:115], v[110:111]
	global_load_dwordx4 v[6:9], v105, s[12:13]
	global_load_dwordx2 v[10:11], v104, s[8:9] nt
	s_add_u32 s8, s8, s16
	s_addc_u32 s9, s9, s17
	s_add_u32 s12, s12, s18
	s_addc_u32 s13, s13, s19
	s_waitcnt vmcnt(45)
	v_lshlrev_b32_e32 v108, 16, v16
	v_and_b32_e32 v109, 0xffff0000, v16
	v_lshlrev_b32_e32 v110, 16, v17
	v_and_b32_e32 v111, 0xffff0000, v17
	v_pk_fma_f32 v[112:113], v[12:13], v[112:113], v[108:109]
	v_pk_fma_f32 v[114:115], v[14:15], v[114:115], v[110:111]
	global_load_dwordx4 v[12:15], v105, s[12:13]
	global_load_dwordx2 v[16:17], v104, s[8:9] nt
	s_add_u32 s8, s8, s16
	s_addc_u32 s9, s9, s17
	s_add_u32 s12, s12, s18
	s_addc_u32 s13, s13, s19
	s_waitcnt vmcnt(45)
	v_cvt_pk_bf16_f32 v106, v112, v113
	v_cvt_pk_bf16_f32 v107, v114, v115
	global_store_dwordx2 v104, v[106:107], s[10:11]
	s_add_u32 s10, s10, s24
	s_addc_u32 s11, s11, s25
	v_lshlrev_b32_e32 v108, 16, v22
	v_and_b32_e32 v109, 0xffff0000, v22
	v_lshlrev_b32_e32 v110, 16, v23
	v_and_b32_e32 v111, 0xffff0000, v23
	v_pk_fma_f32 v[112:113], v[18:19], v[112:113], v[108:109]
	v_pk_fma_f32 v[114:115], v[20:21], v[114:115], v[110:111]
	global_load_dwordx4 v[18:21], v105, s[12:13]
	global_load_dwordx2 v[22:23], v104, s[8:9] nt
	s_add_u32 s8, s8, s16
	s_addc_u32 s9, s9, s17
	s_add_u32 s12, s12, s18
	s_addc_u32 s13, s13, s19
	s_waitcnt vmcnt(45)
	v_lshlrev_b32_e32 v108, 16, v28
	v_and_b32_e32 v109, 0xffff0000, v28
	v_lshlrev_b32_e32 v110, 16, v29
	v_and_b32_e32 v111, 0xffff0000, v29
	v_pk_fma_f32 v[112:113], v[24:25], v[112:113], v[108:109]
	v_pk_fma_f32 v[114:115], v[26:27], v[114:115], v[110:111]
	global_load_dwordx4 v[24:27], v105, s[12:13]
	global_load_dwordx2 v[28:29], v104, s[8:9] nt
	s_add_u32 s8, s8, s16
	s_addc_u32 s9, s9, s17
	s_add_u32 s12, s12, s18
	s_addc_u32 s13, s13, s19
	s_waitcnt vmcnt(45)
	v_cvt_pk_bf16_f32 v106, v112, v113
	v_cvt_pk_bf16_f32 v107, v114, v115
	global_store_dwordx2 v104, v[106:107], s[10:11]
	s_add_u32 s10, s10, s24
	s_addc_u32 s11, s11, s25
	v_lshlrev_b32_e32 v108, 16, v34
	v_and_b32_e32 v109, 0xffff0000, v34
	v_lshlrev_b32_e32 v110, 16, v35
	v_and_b32_e32 v111, 0xffff0000, v35
	v_pk_fma_f32 v[112:113], v[30:31], v[112:113], v[108:109]
	v_pk_fma_f32 v[114:115], v[32:33], v[114:115], v[110:111]
	global_load_dwordx4 v[30:33], v105, s[12:13]
	global_load_dwordx2 v[34:35], v104, s[8:9] nt
	s_add_u32 s8, s8, s16
	s_addc_u32 s9, s9, s17
	s_add_u32 s12, s12, s18
	s_addc_u32 s13, s13, s19
	s_waitcnt vmcnt(45)
	v_lshlrev_b32_e32 v108, 16, v40
	v_and_b32_e32 v109, 0xffff0000, v40
	v_lshlrev_b32_e32 v110, 16, v41
	v_and_b32_e32 v111, 0xffff0000, v41
	v_pk_fma_f32 v[112:113], v[36:37], v[112:113], v[108:109]
	v_pk_fma_f32 v[114:115], v[38:39], v[114:115], v[110:111]
	global_load_dwordx4 v[36:39], v105, s[12:13]
	global_load_dwordx2 v[40:41], v104, s[8:9] nt
	s_add_u32 s8, s8, s16
	s_addc_u32 s9, s9, s17
	s_add_u32 s12, s12, s18
	s_addc_u32 s13, s13, s19
	s_waitcnt vmcnt(45)
	v_cvt_pk_bf16_f32 v106, v112, v113
	v_cvt_pk_bf16_f32 v107, v114, v115
	global_store_dwordx2 v104, v[106:107], s[10:11]
	s_add_u32 s10, s10, s24
	s_addc_u32 s11, s11, s25
	v_lshlrev_b32_e32 v108, 16, v46
	v_and_b32_e32 v109, 0xffff0000, v46
	v_lshlrev_b32_e32 v110, 16, v47
	v_and_b32_e32 v111, 0xffff0000, v47
	v_pk_fma_f32 v[112:113], v[42:43], v[112:113], v[108:109]
	v_pk_fma_f32 v[114:115], v[44:45], v[114:115], v[110:111]
	s_waitcnt vmcnt(43)
	v_lshlrev_b32_e32 v108, 16, v52
	v_and_b32_e32 v109, 0xffff0000, v52
	v_lshlrev_b32_e32 v110, 16, v53
	v_and_b32_e32 v111, 0xffff0000, v53
	v_pk_fma_f32 v[112:113], v[48:49], v[112:113], v[108:109]
	v_pk_fma_f32 v[114:115], v[50:51], v[114:115], v[110:111]
	s_waitcnt vmcnt(41)
	v_cvt_pk_bf16_f32 v106, v112, v113
	v_cvt_pk_bf16_f32 v107, v114, v115
	global_store_dwordx2 v104, v[106:107], s[10:11]
	s_add_u32 s10, s10, s24
	s_addc_u32 s11, s11, s25
	v_lshlrev_b32_e32 v108, 16, v58
	v_and_b32_e32 v109, 0xffff0000, v58
	v_lshlrev_b32_e32 v110, 16, v59
	v_and_b32_e32 v111, 0xffff0000, v59
	v_pk_fma_f32 v[112:113], v[54:55], v[112:113], v[108:109]
	v_pk_fma_f32 v[114:115], v[56:57], v[114:115], v[110:111]
	s_waitcnt vmcnt(39)
	v_lshlrev_b32_e32 v108, 16, v66
	v_and_b32_e32 v109, 0xffff0000, v66
	v_lshlrev_b32_e32 v110, 16, v67
	v_and_b32_e32 v111, 0xffff0000, v67
	v_pk_fma_f32 v[112:113], v[60:61], v[112:113], v[108:109]
	v_pk_fma_f32 v[114:115], v[62:63], v[114:115], v[110:111]
	s_waitcnt vmcnt(37)
	v_cvt_pk_bf16_f32 v106, v112, v113
	v_cvt_pk_bf16_f32 v107, v114, v115
	global_store_dwordx2 v104, v[106:107], s[10:11]
	s_add_u32 s10, s10, s24
	s_addc_u32 s11, s11, s25
	v_lshlrev_b32_e32 v108, 16, v76
	v_and_b32_e32 v109, 0xffff0000, v76
	v_lshlrev_b32_e32 v110, 16, v77
	v_and_b32_e32 v111, 0xffff0000, v77
	v_pk_fma_f32 v[112:113], v[72:73], v[112:113], v[108:109]
	v_pk_fma_f32 v[114:115], v[74:75], v[114:115], v[110:111]
	s_waitcnt vmcnt(35)
	v_lshlrev_b32_e32 v108, 16, v82
	v_and_b32_e32 v109, 0xffff0000, v82
	v_lshlrev_b32_e32 v110, 16, v83
	v_and_b32_e32 v111, 0xffff0000, v83
	v_pk_fma_f32 v[112:113], v[78:79], v[112:113], v[108:109]
	v_pk_fma_f32 v[114:115], v[80:81], v[114:115], v[110:111]
	s_waitcnt vmcnt(33)
	v_cvt_pk_bf16_f32 v106, v112, v113
	v_cvt_pk_bf16_f32 v107, v114, v115
	global_store_dwordx2 v104, v[106:107], s[10:11]
	s_add_u32 s10, s10, s24
	s_addc_u32 s11, s11, s25
	v_lshlrev_b32_e32 v108, 16, v88
	v_and_b32_e32 v109, 0xffff0000, v88
	v_lshlrev_b32_e32 v110, 16, v89
	v_and_b32_e32 v111, 0xffff0000, v89
	v_pk_fma_f32 v[112:113], v[84:85], v[112:113], v[108:109]
	v_pk_fma_f32 v[114:115], v[86:87], v[114:115], v[110:111]
	s_waitcnt vmcnt(31)
	v_lshlrev_b32_e32 v108, 16, v94
	v_and_b32_e32 v109, 0xffff0000, v94
	v_lshlrev_b32_e32 v110, 16, v95
	v_and_b32_e32 v111, 0xffff0000, v95
	v_pk_fma_f32 v[112:113], v[90:91], v[112:113], v[108:109]
	v_pk_fma_f32 v[114:115], v[92:93], v[114:115], v[110:111]
	s_waitcnt vmcnt(29)
	v_cvt_pk_bf16_f32 v106, v112, v113
	v_cvt_pk_bf16_f32 v107, v114, v115
	global_store_dwordx2 v104, v[106:107], s[10:11]
	s_add_u32 s10, s10, s24
	s_addc_u32 s11, s11, s25
	v_lshlrev_b32_e32 v108, 16, v100
	v_and_b32_e32 v109, 0xffff0000, v100
	v_lshlrev_b32_e32 v110, 16, v101
	v_and_b32_e32 v111, 0xffff0000, v101
	v_pk_fma_f32 v[112:113], v[96:97], v[112:113], v[108:109]
	v_pk_fma_f32 v[114:115], v[98:99], v[114:115], v[110:111]
	s_waitcnt vmcnt(27)
	v_lshlrev_b32_e32 v108, 16, v248
	v_and_b32_e32 v109, 0xffff0000, v248
	v_lshlrev_b32_e32 v110, 16, v249
	v_and_b32_e32 v111, 0xffff0000, v249
	v_pk_fma_f32 v[112:113], v[244:245], v[112:113], v[108:109]
	v_pk_fma_f32 v[114:115], v[246:247], v[114:115], v[110:111]
	s_waitcnt vmcnt(25)
	v_cvt_pk_bf16_f32 v106, v112, v113
	v_cvt_pk_bf16_f32 v107, v114, v115
	global_store_dwordx2 v104, v[106:107], s[10:11]
	s_add_u32 s10, s10, s24
	s_addc_u32 s11, s11, s25
	v_lshlrev_b32_e32 v108, 16, v254
	v_and_b32_e32 v109, 0xffff0000, v254
	v_lshlrev_b32_e32 v110, 16, v255
	v_and_b32_e32 v111, 0xffff0000, v255
	v_pk_fma_f32 v[112:113], v[250:251], v[112:113], v[108:109]
	v_pk_fma_f32 v[114:115], v[252:253], v[114:115], v[110:111]
	s_waitcnt vmcnt(23)
	v_lshlrev_b32_e32 v108, 16, v68
	v_and_b32_e32 v109, 0xffff0000, v68
	v_lshlrev_b32_e32 v110, 16, v69
	v_and_b32_e32 v111, 0xffff0000, v69
	v_pk_fma_f32 v[112:113], v[196:197], v[112:113], v[108:109]
	v_pk_fma_f32 v[114:115], v[198:199], v[114:115], v[110:111]
	s_waitcnt vmcnt(21)
	v_cvt_pk_bf16_f32 v106, v112, v113
	v_cvt_pk_bf16_f32 v107, v114, v115
	global_store_dwordx2 v104, v[106:107], s[10:11]
	s_add_u32 s10, s10, s24
	s_addc_u32 s11, s11, s25
	v_lshlrev_b32_e32 v108, 16, v4
	v_and_b32_e32 v109, 0xffff0000, v4
	v_lshlrev_b32_e32 v110, 16, v5
	v_and_b32_e32 v111, 0xffff0000, v5
	v_pk_fma_f32 v[112:113], v[0:1], v[112:113], v[108:109]
	v_pk_fma_f32 v[114:115], v[2:3], v[114:115], v[110:111]
	s_waitcnt vmcnt(19)
	v_lshlrev_b32_e32 v108, 16, v10
	v_and_b32_e32 v109, 0xffff0000, v10
	v_lshlrev_b32_e32 v110, 16, v11
	v_and_b32_e32 v111, 0xffff0000, v11
	v_pk_fma_f32 v[112:113], v[6:7], v[112:113], v[108:109]
	v_pk_fma_f32 v[114:115], v[8:9], v[114:115], v[110:111]
	s_waitcnt vmcnt(17)
	v_cvt_pk_bf16_f32 v106, v112, v113
	v_cvt_pk_bf16_f32 v107, v114, v115
	global_store_dwordx2 v104, v[106:107], s[10:11]
	s_add_u32 s10, s10, s24
	s_addc_u32 s11, s11, s25
	v_lshlrev_b32_e32 v108, 16, v16
	v_and_b32_e32 v109, 0xffff0000, v16
	v_lshlrev_b32_e32 v110, 16, v17
	v_and_b32_e32 v111, 0xffff0000, v17
	v_pk_fma_f32 v[112:113], v[12:13], v[112:113], v[108:109]
	v_pk_fma_f32 v[114:115], v[14:15], v[114:115], v[110:111]
	s_waitcnt vmcnt(15)
	v_lshlrev_b32_e32 v108, 16, v22
	v_and_b32_e32 v109, 0xffff0000, v22
	v_lshlrev_b32_e32 v110, 16, v23
	v_and_b32_e32 v111, 0xffff0000, v23
	v_pk_fma_f32 v[112:113], v[18:19], v[112:113], v[108:109]
	v_pk_fma_f32 v[114:115], v[20:21], v[114:115], v[110:111]
	s_waitcnt vmcnt(13)
	v_cvt_pk_bf16_f32 v106, v112, v113
	v_cvt_pk_bf16_f32 v107, v114, v115
	global_store_dwordx2 v104, v[106:107], s[10:11]
	s_add_u32 s10, s10, s24
	s_addc_u32 s11, s11, s25
	v_lshlrev_b32_e32 v108, 16, v28
	v_and_b32_e32 v109, 0xffff0000, v28
	v_lshlrev_b32_e32 v110, 16, v29
	v_and_b32_e32 v111, 0xffff0000, v29
	v_pk_fma_f32 v[112:113], v[24:25], v[112:113], v[108:109]
	v_pk_fma_f32 v[114:115], v[26:27], v[114:115], v[110:111]
	s_waitcnt vmcnt(11)
	v_lshlrev_b32_e32 v108, 16, v34
	v_and_b32_e32 v109, 0xffff0000, v34
	v_lshlrev_b32_e32 v110, 16, v35
	v_and_b32_e32 v111, 0xffff0000, v35
	v_pk_fma_f32 v[112:113], v[30:31], v[112:113], v[108:109]
	v_pk_fma_f32 v[114:115], v[32:33], v[114:115], v[110:111]
	s_waitcnt vmcnt(9)
	v_cvt_pk_bf16_f32 v106, v112, v113
	v_cvt_pk_bf16_f32 v107, v114, v115
	global_store_dwordx2 v104, v[106:107], s[10:11]
	s_add_u32 s10, s10, s24
	s_addc_u32 s11, s11, s25
	v_lshlrev_b32_e32 v108, 16, v40
	v_and_b32_e32 v109, 0xffff0000, v40
	v_lshlrev_b32_e32 v110, 16, v41
	v_and_b32_e32 v111, 0xffff0000, v41
	v_pk_fma_f32 v[112:113], v[36:37], v[112:113], v[108:109]
	v_pk_fma_f32 v[114:115], v[38:39], v[114:115], v[110:111]
	s_branch .LBB0_636
